# baseline (speedup 1.0000x reference)
.Lk_328:
	s_or_b64 exec, exec, s[0:1]
	s_waitcnt lgkmcnt(0)
	s_and_saveexec_b64 s[4:5], s[42:43]
	s_cbranch_execz .Lk_388
	v_cvt_f32_f64_e32 v3, v[38:39]
	v_cvt_f32_f64_e32 v2, v[36:37]
	v_cvt_f32_f64_e32 v6, v[6:7]
	v_cvt_f32_f64_e32 v4, v[4:5]
	ds_read_b32 v100, v67
	ds_read_b32 v110, v69
	ds_read_b32 v101, v67 offset:2048
	ds_read_b32 v111, v69 offset:2048
	ds_read_b32 v102, v67 offset:4096
	ds_read_b32 v112, v69 offset:4096
	ds_read_b32 v103, v67 offset:6144
	ds_read_b32 v113, v69 offset:6144
	ds_read_b32 v104, v67 offset:8192
	ds_read_b32 v114, v69 offset:8192
	ds_read_b32 v105, v67 offset:10240
	ds_read_b32 v115, v69 offset:10240
	ds_read_b32 v106, v67 offset:12288
	ds_read_b32 v116, v69 offset:12288
	ds_read_b32 v107, v67 offset:14336
	ds_read_b32 v117, v69 offset:14336
	ds_read_b32 v108, v67 offset:16384
	ds_read_b32 v118, v69 offset:16384
	ds_read_b32 v109, v67 offset:18432
	ds_read_b32 v119, v69 offset:18432
	v_lshrrev_b32_e32 v0, 5, v160
	v_mov_b32_e32 v1, 0x25000
	v_lshl_or_b32 v1, v0, 2, v1
	s_mov_b32 s6, 0x80000000
	s_mov_b32 s7, 0x80000000
	s_waitcnt lgkmcnt(0)
	v_mul_f32_e32 v120, v110, v3
	v_mul_f32_e32 v121, v111, v3
	v_mul_f32_e32 v122, v112, v3
	v_mul_f32_e32 v123, v113, v3
	v_mul_f32_e32 v124, v114, v3
	v_mul_f32_e32 v125, v115, v3
	v_mul_f32_e32 v126, v116, v3
	v_mul_f32_e32 v127, v117, v3
	v_mul_f32_e32 v128, v118, v3
	v_mul_f32_e32 v129, v119, v3
	v_fmac_f32_e32 v120, v100, v2
	v_fmac_f32_e32 v121, v101, v2
	v_fmac_f32_e32 v122, v102, v2
	v_fmac_f32_e32 v123, v103, v2
	v_fmac_f32_e32 v124, v104, v2
	v_fmac_f32_e32 v125, v105, v2
	v_fmac_f32_e32 v126, v106, v2
	v_fmac_f32_e32 v127, v107, v2
	v_fmac_f32_e32 v128, v108, v2
	v_fmac_f32_e32 v129, v109, v2
	v_mov_b32_e32 v140, 0
	v_mov_b32_e32 v141, 0
	v_mov_b32_e32 v142, 0
	v_mov_b32_e32 v143, 0
	v_mov_b32_e32 v144, 0
	v_mov_b32_e32 v145, 0
	v_mov_b32_e32 v146, 0
	v_mov_b32_e32 v147, 0
	v_mov_b32_e32 v148, 0
	v_mov_b32_e32 v149, 0
	v_add_f32_dpp v120, v120, v120 row_ror:8 row_mask:0xf bank_mask:0xf bound_ctrl:1
	v_add_f32_dpp v121, v121, v121 row_ror:8 row_mask:0xf bank_mask:0xf bound_ctrl:1
	v_add_f32_dpp v122, v122, v122 row_ror:8 row_mask:0xf bank_mask:0xf bound_ctrl:1
	v_add_f32_dpp v123, v123, v123 row_ror:8 row_mask:0xf bank_mask:0xf bound_ctrl:1
	v_add_f32_dpp v124, v124, v124 row_ror:8 row_mask:0xf bank_mask:0xf bound_ctrl:1
	v_add_f32_dpp v125, v125, v125 row_ror:8 row_mask:0xf bank_mask:0xf bound_ctrl:1
	v_add_f32_dpp v126, v126, v126 row_ror:8 row_mask:0xf bank_mask:0xf bound_ctrl:1
	v_add_f32_dpp v127, v127, v127 row_ror:8 row_mask:0xf bank_mask:0xf bound_ctrl:1
	v_add_f32_dpp v128, v128, v128 row_ror:8 row_mask:0xf bank_mask:0xf bound_ctrl:1
	v_add_f32_dpp v129, v129, v129 row_ror:8 row_mask:0xf bank_mask:0xf bound_ctrl:1
	v_add_f32_dpp v120, v120, v120 row_ror:4 row_mask:0xf bank_mask:0xf bound_ctrl:1
	v_add_f32_dpp v121, v121, v121 row_ror:4 row_mask:0xf bank_mask:0xf bound_ctrl:1
	v_add_f32_dpp v122, v122, v122 row_ror:4 row_mask:0xf bank_mask:0xf bound_ctrl:1
	v_add_f32_dpp v123, v123, v123 row_ror:4 row_mask:0xf bank_mask:0xf bound_ctrl:1
	v_add_f32_dpp v124, v124, v124 row_ror:4 row_mask:0xf bank_mask:0xf bound_ctrl:1
	v_add_f32_dpp v125, v125, v125 row_ror:4 row_mask:0xf bank_mask:0xf bound_ctrl:1
	v_add_f32_dpp v126, v126, v126 row_ror:4 row_mask:0xf bank_mask:0xf bound_ctrl:1
	v_add_f32_dpp v127, v127, v127 row_ror:4 row_mask:0xf bank_mask:0xf bound_ctrl:1
	v_add_f32_dpp v128, v128, v128 row_ror:4 row_mask:0xf bank_mask:0xf bound_ctrl:1
	v_add_f32_dpp v129, v129, v129 row_ror:4 row_mask:0xf bank_mask:0xf bound_ctrl:1
	v_add_f32_dpp v120, v120, v120 row_ror:2 row_mask:0xf bank_mask:0xf bound_ctrl:1
	v_add_f32_dpp v121, v121, v121 row_ror:2 row_mask:0xf bank_mask:0xf bound_ctrl:1
	v_add_f32_dpp v122, v122, v122 row_ror:2 row_mask:0xf bank_mask:0xf bound_ctrl:1
	v_add_f32_dpp v123, v123, v123 row_ror:2 row_mask:0xf bank_mask:0xf bound_ctrl:1
	v_add_f32_dpp v124, v124, v124 row_ror:2 row_mask:0xf bank_mask:0xf bound_ctrl:1
	v_add_f32_dpp v125, v125, v125 row_ror:2 row_mask:0xf bank_mask:0xf bound_ctrl:1
	v_add_f32_dpp v126, v126, v126 row_ror:2 row_mask:0xf bank_mask:0xf bound_ctrl:1
	v_add_f32_dpp v127, v127, v127 row_ror:2 row_mask:0xf bank_mask:0xf bound_ctrl:1
	v_add_f32_dpp v128, v128, v128 row_ror:2 row_mask:0xf bank_mask:0xf bound_ctrl:1
	v_add_f32_dpp v129, v129, v129 row_ror:2 row_mask:0xf bank_mask:0xf bound_ctrl:1
	v_add_f32_dpp v120, v120, v120 row_ror:1 row_mask:0xf bank_mask:0xf bound_ctrl:1
	v_add_f32_dpp v121, v121, v121 row_ror:1 row_mask:0xf bank_mask:0xf bound_ctrl:1
	v_add_f32_dpp v122, v122, v122 row_ror:1 row_mask:0xf bank_mask:0xf bound_ctrl:1
	v_add_f32_dpp v123, v123, v123 row_ror:1 row_mask:0xf bank_mask:0xf bound_ctrl:1
	v_add_f32_dpp v124, v124, v124 row_ror:1 row_mask:0xf bank_mask:0xf bound_ctrl:1
	v_add_f32_dpp v125, v125, v125 row_ror:1 row_mask:0xf bank_mask:0xf bound_ctrl:1
	v_add_f32_dpp v126, v126, v126 row_ror:1 row_mask:0xf bank_mask:0xf bound_ctrl:1
	v_add_f32_dpp v127, v127, v127 row_ror:1 row_mask:0xf bank_mask:0xf bound_ctrl:1
	v_add_f32_dpp v128, v128, v128 row_ror:1 row_mask:0xf bank_mask:0xf bound_ctrl:1
	v_add_f32_dpp v129, v129, v129 row_ror:1 row_mask:0xf bank_mask:0xf bound_ctrl:1
	v_mov_b32_dpp v140, v120 row_bcast:15 row_mask:0xa bank_mask:0xf
	v_mov_b32_dpp v141, v121 row_bcast:15 row_mask:0xa bank_mask:0xf
	v_mov_b32_dpp v142, v122 row_bcast:15 row_mask:0xa bank_mask:0xf
	v_mov_b32_dpp v143, v123 row_bcast:15 row_mask:0xa bank_mask:0xf
	v_mov_b32_dpp v144, v124 row_bcast:15 row_mask:0xa bank_mask:0xf
	v_mov_b32_dpp v145, v125 row_bcast:15 row_mask:0xa bank_mask:0xf
	v_mov_b32_dpp v146, v126 row_bcast:15 row_mask:0xa bank_mask:0xf
	v_mov_b32_dpp v147, v127 row_bcast:15 row_mask:0xa bank_mask:0xf
	v_mov_b32_dpp v148, v128 row_bcast:15 row_mask:0xa bank_mask:0xf
	v_mov_b32_dpp v149, v129 row_bcast:15 row_mask:0xa bank_mask:0xf
	v_add_f32_e32 v120, v120, v140
	v_add_f32_e32 v121, v121, v141
	v_add_f32_e32 v122, v122, v142
	v_add_f32_e32 v123, v123, v143
	v_add_f32_e32 v124, v124, v144
	v_add_f32_e32 v125, v125, v145
	v_add_f32_e32 v126, v126, v146
	v_add_f32_e32 v127, v127, v147
	v_add_f32_e32 v128, v128, v148
	v_add_f32_e32 v129, v129, v149
	s_mov_b64 s[10:11], exec
	s_mov_b64 exec, s[6:7]
	ds_write_b32 v1, v120
	ds_write_b32 v1, v121 offset:32
	ds_write_b32 v1, v122 offset:64
	ds_write_b32 v1, v123 offset:96
	ds_write_b32 v1, v124 offset:128
	ds_write_b32 v1, v125 offset:160
	ds_write_b32 v1, v126 offset:192
	ds_write_b32 v1, v127 offset:224
	ds_write_b32 v1, v128 offset:256
	ds_write_b32 v1, v129 offset:288
	s_mov_b64 exec, s[10:11]
	s_cmpk_gt_u32 s2, 0x7f
	s_cbranch_scc1 .Lmy_ro_done
	v_mul_f32_e32 v130, v110, v4
	v_mul_f32_e32 v131, v111, v4
	v_mul_f32_e32 v132, v112, v4
	v_mul_f32_e32 v133, v113, v4
	v_mul_f32_e32 v134, v114, v4
	v_mul_f32_e32 v135, v115, v4
	v_mul_f32_e32 v136, v116, v4
	v_mul_f32_e32 v137, v117, v4
	v_mul_f32_e32 v138, v118, v4
	v_mul_f32_e32 v139, v119, v4
	v_fmac_f32_e32 v130, v100, v6
	v_fmac_f32_e32 v131, v101, v6
	v_fmac_f32_e32 v132, v102, v6
	v_fmac_f32_e32 v133, v103, v6
	v_fmac_f32_e32 v134, v104, v6
	v_fmac_f32_e32 v135, v105, v6
	v_fmac_f32_e32 v136, v106, v6
	v_fmac_f32_e32 v137, v107, v6
	v_fmac_f32_e32 v138, v108, v6
	v_fmac_f32_e32 v139, v109, v6
	v_mov_b32_e32 v140, 0
	v_mov_b32_e32 v141, 0
	v_mov_b32_e32 v142, 0
	v_mov_b32_e32 v143, 0
	v_mov_b32_e32 v144, 0
	v_mov_b32_e32 v145, 0
	v_mov_b32_e32 v146, 0
	v_mov_b32_e32 v147, 0
	v_mov_b32_e32 v148, 0
	v_mov_b32_e32 v149, 0
	v_add_f32_dpp v130, v130, v130 row_ror:8 row_mask:0xf bank_mask:0xf bound_ctrl:1
	v_add_f32_dpp v131, v131, v131 row_ror:8 row_mask:0xf bank_mask:0xf bound_ctrl:1
	v_add_f32_dpp v132, v132, v132 row_ror:8 row_mask:0xf bank_mask:0xf bound_ctrl:1
	v_add_f32_dpp v133, v133, v133 row_ror:8 row_mask:0xf bank_mask:0xf bound_ctrl:1
	v_add_f32_dpp v134, v134, v134 row_ror:8 row_mask:0xf bank_mask:0xf bound_ctrl:1
	v_add_f32_dpp v135, v135, v135 row_ror:8 row_mask:0xf bank_mask:0xf bound_ctrl:1
	v_add_f32_dpp v136, v136, v136 row_ror:8 row_mask:0xf bank_mask:0xf bound_ctrl:1
	v_add_f32_dpp v137, v137, v137 row_ror:8 row_mask:0xf bank_mask:0xf bound_ctrl:1
	v_add_f32_dpp v138, v138, v138 row_ror:8 row_mask:0xf bank_mask:0xf bound_ctrl:1
	v_add_f32_dpp v139, v139, v139 row_ror:8 row_mask:0xf bank_mask:0xf bound_ctrl:1
	v_add_f32_dpp v130, v130, v130 row_ror:4 row_mask:0xf bank_mask:0xf bound_ctrl:1
	v_add_f32_dpp v131, v131, v131 row_ror:4 row_mask:0xf bank_mask:0xf bound_ctrl:1
	v_add_f32_dpp v132, v132, v132 row_ror:4 row_mask:0xf bank_mask:0xf bound_ctrl:1
	v_add_f32_dpp v133, v133, v133 row_ror:4 row_mask:0xf bank_mask:0xf bound_ctrl:1
	v_add_f32_dpp v134, v134, v134 row_ror:4 row_mask:0xf bank_mask:0xf bound_ctrl:1
	v_add_f32_dpp v135, v135, v135 row_ror:4 row_mask:0xf bank_mask:0xf bound_ctrl:1
	v_add_f32_dpp v136, v136, v136 row_ror:4 row_mask:0xf bank_mask:0xf bound_ctrl:1
	v_add_f32_dpp v137, v137, v137 row_ror:4 row_mask:0xf bank_mask:0xf bound_ctrl:1
	v_add_f32_dpp v138, v138, v138 row_ror:4 row_mask:0xf bank_mask:0xf bound_ctrl:1
	v_add_f32_dpp v139, v139, v139 row_ror:4 row_mask:0xf bank_mask:0xf bound_ctrl:1
	v_add_f32_dpp v130, v130, v130 row_ror:2 row_mask:0xf bank_mask:0xf bound_ctrl:1
	v_add_f32_dpp v131, v131, v131 row_ror:2 row_mask:0xf bank_mask:0xf bound_ctrl:1
	v_add_f32_dpp v132, v132, v132 row_ror:2 row_mask:0xf bank_mask:0xf bound_ctrl:1
	v_add_f32_dpp v133, v133, v133 row_ror:2 row_mask:0xf bank_mask:0xf bound_ctrl:1
	v_add_f32_dpp v134, v134, v134 row_ror:2 row_mask:0xf bank_mask:0xf bound_ctrl:1
	v_add_f32_dpp v135, v135, v135 row_ror:2 row_mask:0xf bank_mask:0xf bound_ctrl:1
	v_add_f32_dpp v136, v136, v136 row_ror:2 row_mask:0xf bank_mask:0xf bound_ctrl:1
	v_add_f32_dpp v137, v137, v137 row_ror:2 row_mask:0xf bank_mask:0xf bound_ctrl:1
	v_add_f32_dpp v138, v138, v138 row_ror:2 row_mask:0xf bank_mask:0xf bound_ctrl:1
	v_add_f32_dpp v139, v139, v139 row_ror:2 row_mask:0xf bank_mask:0xf bound_ctrl:1
	v_add_f32_dpp v130, v130, v130 row_ror:1 row_mask:0xf bank_mask:0xf bound_ctrl:1
	v_add_f32_dpp v131, v131, v131 row_ror:1 row_mask:0xf bank_mask:0xf bound_ctrl:1
	v_add_f32_dpp v132, v132, v132 row_ror:1 row_mask:0xf bank_mask:0xf bound_ctrl:1
	v_add_f32_dpp v133, v133, v133 row_ror:1 row_mask:0xf bank_mask:0xf bound_ctrl:1
	v_add_f32_dpp v134, v134, v134 row_ror:1 row_mask:0xf bank_mask:0xf bound_ctrl:1
	v_add_f32_dpp v135, v135, v135 row_ror:1 row_mask:0xf bank_mask:0xf bound_ctrl:1
	v_add_f32_dpp v136, v136, v136 row_ror:1 row_mask:0xf bank_mask:0xf bound_ctrl:1
	v_add_f32_dpp v137, v137, v137 row_ror:1 row_mask:0xf bank_mask:0xf bound_ctrl:1
	v_add_f32_dpp v138, v138, v138 row_ror:1 row_mask:0xf bank_mask:0xf bound_ctrl:1
	v_add_f32_dpp v139, v139, v139 row_ror:1 row_mask:0xf bank_mask:0xf bound_ctrl:1
	v_mov_b32_dpp v140, v130 row_bcast:15 row_mask:0xa bank_mask:0xf
	v_mov_b32_dpp v141, v131 row_bcast:15 row_mask:0xa bank_mask:0xf
	v_mov_b32_dpp v142, v132 row_bcast:15 row_mask:0xa bank_mask:0xf
	v_mov_b32_dpp v143, v133 row_bcast:15 row_mask:0xa bank_mask:0xf
	v_mov_b32_dpp v144, v134 row_bcast:15 row_mask:0xa bank_mask:0xf
	v_mov_b32_dpp v145, v135 row_bcast:15 row_mask:0xa bank_mask:0xf
	v_mov_b32_dpp v146, v136 row_bcast:15 row_mask:0xa bank_mask:0xf
	v_mov_b32_dpp v147, v137 row_bcast:15 row_mask:0xa bank_mask:0xf
	v_mov_b32_dpp v148, v138 row_bcast:15 row_mask:0xa bank_mask:0xf
	v_mov_b32_dpp v149, v139 row_bcast:15 row_mask:0xa bank_mask:0xf
	v_add_f32_e32 v130, v130, v140
	v_add_f32_e32 v131, v131, v141
	v_add_f32_e32 v132, v132, v142
	v_add_f32_e32 v133, v133, v143
	v_add_f32_e32 v134, v134, v144
	v_add_f32_e32 v135, v135, v145
	v_add_f32_e32 v136, v136, v146
	v_add_f32_e32 v137, v137, v147
	v_add_f32_e32 v138, v138, v148
	v_add_f32_e32 v139, v139, v149
	s_mov_b64 exec, s[6:7]
	ds_write_b32 v1, v130 offset:320
	ds_write_b32 v1, v131 offset:352
	ds_write_b32 v1, v132 offset:384
	ds_write_b32 v1, v133 offset:416
	ds_write_b32 v1, v134 offset:448
	ds_write_b32 v1, v135 offset:480
	ds_write_b32 v1, v136 offset:512
	ds_write_b32 v1, v137 offset:544
	ds_write_b32 v1, v138 offset:576
	ds_write_b32 v1, v139 offset:608
	s_mov_b64 exec, s[10:11]
